# prologue restructured: tile 0 issued before weights, tiles 1-2 issued right after first weight half; second Wk half reloaded into dead Wq registers; 4-buffer ring loop; nt mask loads
# baseline (speedup 1.0000x reference)
_Z10k_attn_epiILi2EEvPKfS1_PKiPKDF16_S5_PfS1_S1_S5_S1_S1_S1_S1_S1_S6_:
	s_load_dwordx8 s[12:19], s[0:1], 0x0
	s_load_dwordx2 s[4:5], s[0:1], 0x20
	s_load_dwordx4 s[20:23], s[0:1], 0x30
	v_and_b32_e32 v196, 63, v0
	v_cmp_gt_u32_e64 s[6:7], 32, v196
	s_waitcnt lgkmcnt(0)
	v_mov_b32_e32 v1, s15
	v_mov_b32_e32 v2, s13
	v_lshrrev_b32_e32 v197, 6, v0
	s_lshl_b32 s31, s2, 3
	v_cndmask_b32_e64 v103, v1, v2, s[6:7]
	v_mov_b32_e32 v1, s14
	v_mov_b32_e32 v2, s12
	v_or_b32_e32 v104, s31, v197
	v_cndmask_b32_e64 v102, v1, v2, s[6:7]
	s_mov_b32 s8, 0x19000
	v_lshlrev_b32_e32 v1, 4, v0
	v_mad_i64_i32 v[2:3], s[2:3], v104, s8, v[102:103]
	v_and_b32_e32 v108, 0x1f0, v1
	v_mov_b32_e32 v109, 0
	v_lshl_add_u64 v[14:15], v[2:3], 0, v[108:109]
	v_mov_b32_e32 v2, s23
	v_mov_b32_e32 v3, s21
	v_ashrrev_i32_e32 v105, 31, v104
	v_cndmask_b32_e64 v3, v2, v3, s[6:7]
	v_mov_b32_e32 v2, s22
	v_mov_b32_e32 v4, s20
	v_cndmask_b32_e64 v2, v2, v4, s[6:7]
	v_lshlrev_b64 v[4:5], 9, v[104:105]
	v_lshl_add_u64 v[2:3], v[2:3], 0, v[4:5]
	v_lshlrev_b32_e32 v122, 10, v197
	v_lshl_add_u64 v[2:3], v[2:3], 0, v[108:109]
	v_or_b32_e32 v106, v122, v196
	global_load_dwordx4 v[82:85], v[2:3], off
	s_mov_b64 s[2:3], 0x1000
	v_lshl_add_u64 v[218:219], v[14:15], 0, s[2:3]
	s_movk_i32 s2, 0xc8
	v_bfe_u32 v1, v0, 3, 3
	v_mad_i64_i32 v[182:183], s[2:3], v104, s2, 0
	v_lshlrev_b32_e32 v108, 2, v1
	v_lshl_add_u64 v[2:3], v[182:183], 2, s[16:17]
	v_lshl_add_u64 v[16:17], v[2:3], 0, v[108:109]
	v_lshl_add_u64 v[180:181], v[16:17], 0, 32
	global_load_dword v107, v[16:17], off nt
	global_load_dwordx4 v[70:73], v[14:15], off nt
	global_load_dwordx4 v[66:69], v[14:15], off offset:512 nt
	global_load_dwordx4 v[62:65], v[14:15], off offset:1024 nt
	global_load_dwordx4 v[58:61], v[14:15], off offset:1536 nt
	global_load_dwordx4 v[54:57], v[14:15], off offset:2048 nt
	global_load_dwordx4 v[46:49], v[14:15], off offset:2560 nt
	global_load_dwordx4 v[34:37], v[14:15], off offset:3072 nt
	s_nop 0
	global_load_dwordx4 v[14:17], v[14:15], off offset:3584 nt
	v_lshlrev_b32_e32 v2, 4, v106
	v_or_b32_e32 v123, 0x100, v122
	global_load_dwordx4 v[86:89], v2, s[18:19]
	global_load_dwordx4 v[90:93], v2, s[18:19] offset:1024
	global_load_dwordx4 v[94:97], v2, s[18:19] offset:2048
	global_load_dwordx4 v[98:101], v2, s[18:19] offset:3072
	v_or_b32_e32 v2, v123, v196
	v_or_b32_e32 v124, 0x140, v122
	v_lshlrev_b32_e32 v131, 4, v2
	v_or_b32_e32 v2, v124, v196
	v_or_b32_e32 v125, 0x180, v122
	v_lshlrev_b32_e32 v132, 4, v2
	v_or_b32_e32 v2, v125, v196
	v_or_b32_e32 v126, 0x1c0, v122
	v_lshlrev_b32_e32 v133, 4, v2
	v_or_b32_e32 v2, v126, v196
	v_or_b32_e32 v127, 0x200, v122
	v_lshlrev_b32_e32 v134, 4, v2
	v_or_b32_e32 v2, v127, v196
	v_or_b32_e32 v128, 0x240, v122
	v_lshlrev_b32_e32 v135, 4, v2
	v_or_b32_e32 v2, v128, v196
	v_or_b32_e32 v129, 0x280, v122
	v_lshlrev_b32_e32 v137, 4, v2
	v_or_b32_e32 v2, v129, v196
	v_or_b32_e32 v130, 0x2c0, v122
	v_lshlrev_b32_e32 v136, 4, v2
	v_or_b32_e32 v2, v130, v196
	v_or_b32_e32 v192, 0x300, v122
	v_lshlrev_b32_e32 v142, 4, v2
	v_or_b32_e32 v2, v192, v196
	v_or_b32_e32 v202, 0x340, v122
	v_lshlrev_b32_e32 v143, 4, v2
	v_or_b32_e32 v2, v202, v196
	v_or_b32_e32 v203, 0x380, v122
	v_lshlrev_b32_e32 v144, 4, v2
	v_or_b32_e32 v2, v203, v196
	v_or_b32_e32 v204, 0x3c0, v122
	v_lshlrev_b32_e32 v145, 4, v2
	v_or_b32_e32 v2, v204, v196
	v_lshlrev_b32_e32 v150, 4, v2
	v_lshlrev_b32_e32 v1, 9, v197
	v_or_b32_e32 v3, v1, v196
	v_or_b32_e32 v2, 0x100, v1
	v_lshlrev_b32_e32 v3, 4, v3
	global_load_dwordx4 v[110:113], v131, s[18:19]
	global_load_dwordx4 v[114:117], v132, s[18:19]
	global_load_dwordx4 v[118:121], v133, s[18:19]
	global_load_dwordx4 v[138:141], v134, s[18:19]
	global_load_dwordx4 v[146:149], v135, s[18:19]
	global_load_dwordx4 v[152:155], v137, s[18:19]
	global_load_dwordx4 v[156:159], v136, s[18:19]
	global_load_dwordx4 v[160:163], v142, s[18:19]
	global_load_dwordx4 v[164:167], v143, s[18:19]
	global_load_dwordx4 v[168:171], v144, s[18:19]
	global_load_dwordx4 v[172:175], v145, s[18:19]
	global_load_dwordx4 v[176:179], v150, s[18:19]
	global_load_dwordx4 v[186:189], v3, s[4:5]
	global_load_dwordx4 v[206:209], v3, s[4:5] offset:1024
	global_load_dwordx4 v[210:213], v3, s[4:5] offset:2048
	global_load_dwordx4 v[214:217], v3, s[4:5] offset:3072
	v_or_b32_e32 v3, v2, v196
	v_or_b32_e32 v4, 0x140, v1
	v_lshlrev_b32_e32 v3, 4, v3
	v_or_b32_e32 v5, v4, v196
	v_or_b32_e32 v10, 0x180, v1
	v_or_b32_e32 v12, 0x1000, v196
	v_lshlrev_b32_e32 v5, 4, v5
	v_or_b32_e32 v3, v10, v196
	v_or_b32_e32 v11, 0x1c0, v1
	v_or_b32_e32 v1, v1, v12
	v_lshlrev_b32_e32 v3, 4, v3
	v_or_b32_e32 v5, v11, v196
	v_lshlrev_b32_e32 v1, 4, v1
	v_lshlrev_b32_e32 v5, 4, v5
	global_load_dwordx4 v[78:81], v3, s[4:5]
	global_load_dwordx4 v[74:77], v5, s[4:5]
	v_or_b32_e32 v1, v2, v12
	v_or_b32_e32 v2, v4, v12
	v_lshlrev_b32_e32 v1, 4, v1
	v_lshlrev_b32_e32 v6, 4, v2
	s_nop 0
	global_load_dwordx4 v[6:9], v6, s[4:5]
	v_or_b32_e32 v1, v10, v12
	v_or_b32_e32 v10, v11, v12
	v_lshlrev_b32_e32 v1, 4, v1
	v_lshlrev_b32_e32 v10, 4, v10
	s_nop 0
	global_load_dwordx4 v[10:13], v10, s[4:5]
	s_nop 0
	global_load_dword v151, v[180:181], off nt
	global_load_dwordx4 v[220:223], v[218:219], off nt
	global_load_dwordx4 v[224:227], v[218:219], off offset:512 nt
	global_load_dwordx4 v[228:231], v[218:219], off offset:1024 nt
	global_load_dwordx4 v[232:235], v[218:219], off offset:1536 nt
	global_load_dwordx4 v[236:239], v[218:219], off offset:2048 nt
	global_load_dwordx4 v[240:243], v[218:219], off offset:2560 nt
	global_load_dwordx4 v[244:247], v[218:219], off offset:3072 nt
	global_load_dwordx4 v[248:251], v[218:219], off offset:3584 nt
	s_mov_b64 s[2:3], 0x1000
	v_lshl_add_u64 v[218:219], v[218:219], 0, s[2:3]
	v_lshl_add_u64 v[180:181], v[180:181], 0, 32
	global_load_dword v193, v[180:181], off nt
	global_load_dwordx4 v[50:53], v[218:219], off nt
	global_load_dwordx4 v[42:45], v[218:219], off offset:512 nt
	global_load_dwordx4 v[38:41], v[218:219], off offset:1024 nt
	global_load_dwordx4 v[30:33], v[218:219], off offset:1536 nt
	global_load_dwordx4 v[26:29], v[218:219], off offset:2048 nt
	global_load_dwordx4 v[22:25], v[218:219], off offset:2560 nt
	global_load_dwordx4 v[18:21], v[218:219], off offset:3072 nt
	global_load_dwordx4 v[252:255], v[218:219], off offset:3584 nt
	v_bfe_u32 v195, v0, 4, 2
	v_and_b32_e32 v1, 15, v0
	s_waitcnt vmcnt(51)
	v_cvt_pk_f16_f32 v85, v84, v85
	v_cvt_pk_f16_f32 v84, v82, v83
	v_lshlrev_b32_e32 v82, 3, v196
	s_movk_i32 s2, 0x410
	v_mad_u32_u24 v185, v197, s2, v82
	v_and_b32_e32 v82, 7, v0
	v_and_b32_e32 v194, 48, v0
	v_mad_u32_u24 v105, v82, s2, v194
	ds_write_b64 v185, v[84:85]
	s_waitcnt lgkmcnt(0)
	s_barrier
	ds_read_b128 v[82:85], v105
	ds_read_b128 v[198:201], v105 offset:64
	s_waitcnt vmcnt(41) lgkmcnt(1)
	v_mfma_f32_16x16x32_f16 v[86:89], v[82:85], v[86:89], 0
	s_movk_i32 s2, 0x840
	s_waitcnt vmcnt(33)
	v_mfma_f32_16x16x32_f16 v[82:85], v[82:85], v[146:149], 0
	s_waitcnt lgkmcnt(0)
	v_mfma_f32_16x16x32_f16 v[86:89], v[198:201], v[90:93], v[86:89]
	ds_read_b128 v[90:93], v105 offset:128
	ds_read_b128 v[146:149], v105 offset:192
	s_waitcnt vmcnt(32)
	v_mfma_f32_16x16x32_f16 v[82:85], v[198:201], v[152:155], v[82:85]
	v_lshlrev_b32_e32 v200, 7, v197
	v_lshl_or_b32 v109, v1, 2, v200
	v_add_u32_e32 v109, 0x4100, v109
	s_waitcnt lgkmcnt(1)
	v_mfma_f32_16x16x32_f16 v[86:89], v[90:93], v[94:97], v[86:89]
	ds_read_b128 v[94:97], v105 offset:320
	v_lshl_add_u32 v109, v195, 13, v109
	s_waitcnt vmcnt(31)
	v_mfma_f32_16x16x32_f16 v[82:85], v[90:93], v[156:159], v[82:85]
	ds_read_b128 v[90:93], v105 offset:256
	s_waitcnt lgkmcnt(2)
	v_mfma_f32_16x16x32_f16 v[86:89], v[146:149], v[98:101], v[86:89]
	ds_read_b128 v[98:101], v105 offset:384
	s_waitcnt vmcnt(30)
	v_mfma_f32_16x16x32_f16 v[82:85], v[146:149], v[160:163], v[82:85]
	s_waitcnt lgkmcnt(1)
	v_mfma_f32_16x16x32_f16 v[86:89], v[90:93], v[110:113], v[86:89]
	ds_read_b128 v[110:113], v105 offset:448
	v_and_b32_e32 v105, 0x1c0, v0
	v_mfma_f32_16x16x32_f16 v[86:89], v[94:97], v[114:117], v[86:89]
	s_waitcnt vmcnt(29)
	v_mfma_f32_16x16x32_f16 v[82:85], v[90:93], v[164:167], v[82:85]
	v_mad_u32_u24 v90, v195, s2, v105
	v_lshl_or_b32 v105, v1, 1, v90
	s_movk_i32 s2, 0x210
	s_waitcnt lgkmcnt(1)
	v_mfma_f32_16x16x32_f16 v[86:89], v[98:101], v[118:121], v[86:89]
	s_waitcnt vmcnt(28)
	v_mfma_f32_16x16x32_f16 v[82:85], v[94:97], v[168:171], v[82:85]
	s_waitcnt lgkmcnt(0)
	v_mfma_f32_16x16x32_f16 v[86:89], v[110:113], v[138:141], v[86:89]
	s_waitcnt vmcnt(27)
	v_mfma_f32_16x16x32_f16 v[82:85], v[98:101], v[172:175], v[82:85]
	s_waitcnt vmcnt(26)
	v_mfma_f32_16x16x32_f16 v[82:85], v[110:113], v[176:179], v[82:85]
	s_add_u32 s70, s4, 0x1000
	s_addc_u32 s71, s5, 0
	s_add_u32 s72, s4, 0x10000
	s_addc_u32 s73, s5, 0
	s_add_u32 s74, s4, 0x11000
	s_addc_u32 s75, s5, 0
	v_lshlrev_b32_e32 v2, 13, v197
	v_lshl_or_b32 v2, v196, 4, v2
	global_load_dwordx4 v[110:113], v2, s[70:71]
	global_load_dwordx4 v[114:117], v2, s[70:71] offset:1024
	global_load_dwordx4 v[118:121], v2, s[72:73]
	global_load_dwordx4 v[138:141], v2, s[72:73] offset:1024
	global_load_dwordx4 v[146:149], v2, s[72:73] offset:2048
	global_load_dwordx4 v[152:155], v2, s[72:73] offset:3072
	global_load_dwordx4 v[156:159], v2, s[74:75]
	global_load_dwordx4 v[160:163], v2, s[74:75] offset:2048
	s_nop 3
	v_cvt_f16_f32_e32 v86, v86
	ds_write_b16 v105, v86 offset:58624
	v_cvt_f16_f32_e32 v86, v87
	s_nop 0
	v_cvt_f16_f32_e32 v82, v82
	v_cvt_f16_f32_e32 v87, v88
	v_cvt_f16_f32_e32 v83, v83
	v_cvt_f16_f32_e32 v88, v89
	v_cvt_f16_f32_e32 v84, v84
	v_cvt_f16_f32_e32 v85, v85
	ds_write_b16 v105, v86 offset:59152
	ds_write_b16 v105, v87 offset:59680
	ds_write_b16 v105, v88 offset:60208
	ds_write_b16 v105, v82 offset:58656
	ds_write_b16 v105, v83 offset:59184
	ds_write_b16 v105, v84 offset:59712
	ds_write_b16 v105, v85 offset:60240
	v_mov_b32_e32 v82, 0xe500
	v_mad_u32_u24 v82, v1, s2, v82
	v_add_u32_e32 v198, v82, v194
	s_waitcnt lgkmcnt(0)
	s_barrier
	ds_read_b128 v[82:85], v198
	ds_read_b128 v[86:89], v198 offset:64
	s_waitcnt vmcnt(33) lgkmcnt(1)
	v_mfma_f32_16x16x32_f16 v[94:97], v[82:85], v[186:189], 0
	ds_read_b128 v[90:93], v198 offset:128
	s_waitcnt vmcnt(32) lgkmcnt(1)
	v_mfma_f32_16x16x32_f16 v[98:101], v[86:89], v[206:209], v[94:97]
	s_nop 4
	ds_read_b128 v[94:97], v198 offset:192
	s_waitcnt vmcnt(31) lgkmcnt(1)
	v_mfma_f32_16x16x32_f16 v[98:101], v[90:93], v[210:213], v[98:101]
	s_waitcnt vmcnt(30) lgkmcnt(0)
	v_mfma_f32_16x16x32_f16 v[98:101], v[94:97], v[214:217], v[98:101]
	s_and_saveexec_b64 s[2:3], s[6:7]
	s_cbranch_execz .LBB1_2
	s_nop 5
	v_mul_f32_e32 v98, 0x3e0293ee, v98
	v_mul_f32_e32 v99, 0x3e0293ee, v99
	ds_write2st64_b32 v109, v98, v99 offset1:8
	v_mul_f32_e32 v98, 0x3e0293ee, v100
	v_mul_f32_e32 v99, 0x3e0293ee, v101
	ds_write2st64_b32 v109, v98, v99 offset0:16 offset1:24
.LBB1_2:
	s_or_b64 exec, exec, s[2:3]
	s_waitcnt vmcnt(7)
	v_mfma_f32_16x16x32_f16 v[110:113], v[82:85], v[110:113], 0
	s_waitcnt vmcnt(6)
	v_mfma_f32_16x16x32_f16 v[110:113], v[86:89], v[114:117], v[110:113]
	s_waitcnt vmcnt(29)
	v_mfma_f32_16x16x32_f16 v[110:113], v[90:93], v[78:81], v[110:113]
	v_mad_i64_i32 v[78:79], s[2:3], v104, s8, 0
	s_waitcnt vmcnt(28)
	v_mfma_f32_16x16x32_f16 v[110:113], v[94:97], v[74:77], v[110:113]
	s_and_saveexec_b64 s[2:3], s[6:7]
	s_cbranch_execz .LBB1_4
	s_nop 5
	v_mul_f32_e32 v110, 0x3e0293ee, v110
	v_mul_f32_e32 v111, 0x3e0293ee, v111
	v_add_u32_e32 v114, 64, v109
	ds_write2st64_b32 v114, v110, v111 offset1:8
	v_mul_f32_e32 v110, 0x3e0293ee, v112
	v_mul_f32_e32 v111, 0x3e0293ee, v113
	ds_write2st64_b32 v114, v110, v111 offset0:16 offset1:24
.LBB1_4:
	s_or_b64 exec, exec, s[2:3]
	s_nop 4
	ds_read_b128 v[110:113], v198 offset:256
	ds_read_b128 v[114:117], v198 offset:320
	s_waitcnt vmcnt(5) lgkmcnt(1)
	v_mfma_f32_16x16x32_f16 v[74:77], v[110:113], v[118:121], 0
	ds_read_b128 v[118:121], v198 offset:384
	s_waitcnt vmcnt(4) lgkmcnt(1)
	v_mfma_f32_16x16x32_f16 v[74:77], v[114:117], v[138:141], v[74:77]
	ds_read_b128 v[138:141], v198 offset:448
	s_waitcnt vmcnt(3) lgkmcnt(1)
	v_mfma_f32_16x16x32_f16 v[146:149], v[118:121], v[146:149], v[74:77]
	s_waitcnt vmcnt(2) lgkmcnt(0)
	v_mfma_f32_16x16x32_f16 v[146:149], v[138:141], v[152:155], v[146:149]
	s_and_saveexec_b64 s[2:3], s[6:7]
	s_cbranch_execz .LBB1_6
	s_nop 5
	v_mul_f32_e32 v146, 0x3e0293ee, v146
	v_mul_f32_e32 v147, 0x3e0293ee, v147
	ds_write2st64_b32 v109, v146, v147 offset0:4 offset1:12
	v_mul_f32_e32 v146, 0x3e0293ee, v148
	v_mul_f32_e32 v147, 0x3e0293ee, v149
	ds_write2st64_b32 v109, v146, v147 offset0:20 offset1:28
.LBB1_6:
	s_or_b64 exec, exec, s[2:3]
	s_waitcnt vmcnt(1)
	v_mfma_f32_16x16x32_f16 v[156:159], v[110:113], v[156:159], 0
	s_load_dwordx4 s[24:27], s[0:1], 0x60
	s_load_dwordx8 s[8:15], s[0:1], 0x40
	s_load_dwordx2 s[28:29], s[0:1], 0x28
	v_lshlrev_b32_e32 v184, 2, v196
	s_waitcnt vmcnt(27)
	v_mfma_f32_16x16x32_f16 v[156:159], v[114:117], v[6:9], v[156:159]
	s_waitcnt vmcnt(0)
	v_mfma_f32_16x16x32_f16 v[156:159], v[118:121], v[160:163], v[156:159]
	s_waitcnt vmcnt(26)
	v_mfma_f32_16x16x32_f16 v[156:159], v[138:141], v[10:13], v[156:159]
	s_and_saveexec_b64 s[2:3], s[6:7]
	s_cbranch_execz .LBB1_8
	s_nop 5
	v_mul_f32_e32 v156, 0x3e0293ee, v156
	v_mul_f32_e32 v157, 0x3e0293ee, v157
	v_add_u32_e32 v6, 64, v109
	ds_write2st64_b32 v6, v156, v157 offset0:4 offset1:12
	v_mul_f32_e32 v156, 0x3e0293ee, v158
	v_mul_f32_e32 v157, 0x3e0293ee, v159
	ds_write2st64_b32 v6, v156, v157 offset0:20 offset1:28
.LBB1_8:
	s_or_b64 exec, exec, s[2:3]
	s_nop 4
	v_lshlrev_b32_e32 v156, 11, v197
	v_lshl_or_b32 v156, v184, 2, v156
	s_waitcnt lgkmcnt(0)
	s_barrier
	ds_read_b128 v[10:13], v156 offset:16640
	ds_read_b128 v[6:9], v156 offset:17664
	v_and_b32_e32 v2, 8, v0
	v_cmp_eq_u32_e64 s[4:5], 0, v2
	v_and_b32_e32 v2, 4, v0
	s_load_dwordx2 s[18:19], s[0:1], 0x70
	v_cmp_eq_u32_e64 s[2:3], 0, v2
	v_and_b32_e32 v2, 3, v0
	s_movk_i32 s0, 0x320
	v_cmp_eq_u32_e32 vcc, 0, v2
	v_mad_i64_i32 v[2:3], s[0:1], v104, s0, 0
	v_or_b32_e32 v2, v2, v108
	v_bfe_u32 v109, v0, 2, 1
	v_lshl_add_u64 v[2:3], s[16:17], 0, v[2:3]
	v_lshl_add_u64 v[118:119], v[2:3], 0, 64
	v_lshl_add_u64 v[118:119], v[118:119], 0, 32
	v_mul_u32_u24_e32 v2, 0x320, v109
	s_movk_i32 s0, 0x640
	v_mad_u32_u24 v2, v197, s0, v2
	v_and_b32_e32 v199, 31, v0
	v_or_b32_e32 v2, v2, v108
	v_lshlrev_b32_e32 v186, 4, v199
	v_mov_b32_e32 v187, 0
	v_add_u32_e32 v114, 0x8200, v2
	v_lshl_add_u64 v[2:3], v[78:79], 0, v[186:187]
	v_lshl_add_u64 v[2:3], v[102:103], 0, v[2:3]
	s_mov_b64 s[0:1], 0x3000
	v_add_u32_e32 v201, 0xe500, v105
	v_lshl_add_u64 v[116:117], v[2:3], 0, s[0:1]
	v_mov_b32_e32 v104, 0xff800000
	v_mov_b32_e32 v113, 0xd01502f9
	s_mov_b64 s[16:17], 0x1000
	v_mov_b32_e32 v96, 0
	v_mov_b32_e32 v97, 0
	v_mov_b32_e32 v98, 0
	v_mov_b32_e32 v99, 0
	v_mov_b32_e32 v100, 0
	v_mov_b32_e32 v101, 0
	v_mov_b32_e32 v102, 0
	v_mov_b32_e32 v103, 0
	v_mov_b32_e32 v105, 0
	s_mov_b32 s30, 0
	global_load_dword v205, v[118:119], off nt
	global_load_dwordx4 v[138:141], v[116:117], off nt
	global_load_dwordx4 v[146:149], v[116:117], off offset:512 nt
	global_load_dwordx4 v[152:155], v[116:117], off offset:1024 nt
	global_load_dwordx4 v[156:159], v[116:117], off offset:1536 nt
	global_load_dwordx4 v[160:163], v[116:117], off offset:2048 nt
	global_load_dwordx4 v[164:167], v[116:117], off offset:2560 nt
	global_load_dwordx4 v[168:171], v[116:117], off offset:3072 nt
	global_load_dwordx4 v[172:175], v[116:117], off offset:3584 nt
	v_lshl_add_u64 v[116:117], v[116:117], 0, s[16:17]
	v_lshl_add_u64 v[118:119], v[118:119], 0, 32
	s_waitcnt lgkmcnt(0)

.Lring_go_0:
	v_mul_f32_e32 v74, v10, v70
	v_mul_f32_e32 v75, v6, v70
	v_mul_f32_e32 v76, v10, v66
	v_mul_f32_e32 v77, v6, v66
	v_mul_f32_e32 v78, v10, v62
	v_mul_f32_e32 v79, v6, v62
	v_mul_f32_e32 v80, v10, v58
	v_mul_f32_e32 v81, v6, v58
	v_mul_f32_e32 v82, v10, v54
	v_mul_f32_e32 v83, v6, v54
	v_mul_f32_e32 v84, v10, v46
	v_mul_f32_e32 v85, v6, v46
	v_mul_f32_e32 v86, v10, v34
	v_mul_f32_e32 v87, v6, v34
	v_mul_f32_e32 v88, v10, v14
	v_mul_f32_e32 v89, v6, v14
	v_fmac_f32_e32 v74, v71, v11
	v_fmac_f32_e32 v75, v71, v7
	v_fmac_f32_e32 v76, v67, v11
	v_fmac_f32_e32 v77, v67, v7
	v_fmac_f32_e32 v78, v63, v11
	v_fmac_f32_e32 v79, v63, v7
	v_fmac_f32_e32 v80, v59, v11
	v_fmac_f32_e32 v81, v59, v7
	v_fmac_f32_e32 v82, v55, v11
	v_fmac_f32_e32 v83, v55, v7
	v_fmac_f32_e32 v84, v47, v11
	v_fmac_f32_e32 v85, v47, v7
	v_fmac_f32_e32 v86, v35, v11
	v_fmac_f32_e32 v87, v35, v7
	v_fmac_f32_e32 v88, v15, v11
	v_fmac_f32_e32 v89, v15, v7
	v_fmac_f32_e32 v74, v72, v12
	v_fmac_f32_e32 v75, v72, v8
	v_fmac_f32_e32 v76, v68, v12
	v_fmac_f32_e32 v77, v68, v8
	v_fmac_f32_e32 v78, v64, v12
	v_fmac_f32_e32 v79, v64, v8
	v_fmac_f32_e32 v80, v60, v12
	v_fmac_f32_e32 v81, v60, v8
	v_fmac_f32_e32 v82, v56, v12
	v_fmac_f32_e32 v83, v56, v8
	v_fmac_f32_e32 v84, v48, v12
	v_fmac_f32_e32 v85, v48, v8
	v_fmac_f32_e32 v86, v36, v12
	v_fmac_f32_e32 v87, v36, v8
	v_fmac_f32_e32 v88, v16, v12
	v_fmac_f32_e32 v89, v16, v8
	v_fmac_f32_e32 v74, v73, v13
	v_fmac_f32_e32 v75, v73, v9
	v_fmac_f32_e32 v76, v69, v13
	v_fmac_f32_e32 v77, v69, v9
	v_fmac_f32_e32 v78, v65, v13
	v_fmac_f32_e32 v79, v65, v9
	v_fmac_f32_e32 v80, v61, v13
	v_fmac_f32_e32 v81, v61, v9
	v_fmac_f32_e32 v82, v57, v13
	v_fmac_f32_e32 v83, v57, v9
	v_fmac_f32_e32 v84, v49, v13
	v_fmac_f32_e32 v85, v49, v9
	v_fmac_f32_e32 v86, v37, v13
	v_fmac_f32_e32 v87, v37, v9
	v_fmac_f32_e32 v88, v17, v13
	v_fmac_f32_e32 v89, v17, v9
	v_permlane32_swap_b32_e32 v74, v82
	v_permlane32_swap_b32_e32 v75, v83
	v_permlane32_swap_b32_e32 v76, v84
	v_permlane32_swap_b32_e32 v77, v85
	v_permlane32_swap_b32_e32 v78, v86
	v_permlane32_swap_b32_e32 v79, v87
	v_permlane32_swap_b32_e32 v80, v88
	v_permlane32_swap_b32_e32 v81, v89
	v_add_f32_e32 v74, v74, v82
	v_add_f32_e32 v75, v75, v83
	v_add_f32_e32 v76, v76, v84
	v_add_f32_e32 v77, v77, v85
	v_add_f32_e32 v78, v78, v86
	v_add_f32_e32 v79, v79, v87
	v_add_f32_e32 v80, v80, v88
	v_add_f32_e32 v81, v81, v89
	v_permlane16_swap_b32_e32 v74, v78
	v_permlane16_swap_b32_e32 v75, v79
	v_permlane16_swap_b32_e32 v76, v80
	v_permlane16_swap_b32_e32 v77, v81
	v_add_f32_e32 v74, v74, v78
	v_add_f32_e32 v75, v75, v79
	v_add_f32_e32 v76, v76, v80
	v_add_f32_e32 v77, v77, v81
	v_add_f32_dpp v74, v74, v74 row_ror:8 row_mask:0xf bank_mask:0xf bound_ctrl:1
	v_add_f32_dpp v76, v76, v76 row_ror:8 row_mask:0xf bank_mask:0xf bound_ctrl:1
	v_add_f32_dpp v75, v75, v75 row_ror:8 row_mask:0xf bank_mask:0xf bound_ctrl:1
	v_add_f32_dpp v77, v77, v77 row_ror:8 row_mask:0xf bank_mask:0xf bound_ctrl:1
	v_cndmask_b32_e64 v74, v76, v74, s[4:5]
	v_cndmask_b32_e64 v75, v77, v75, s[4:5]
	v_cmp_eq_u32_e64 s[0:1], 0, v107
	v_add_f32_dpp v74, v74, v74 row_half_mirror row_mask:0xf bank_mask:0xf bound_ctrl:1
	v_add_f32_dpp v75, v75, v75 row_half_mirror row_mask:0xf bank_mask:0xf bound_ctrl:1
	v_cndmask_b32_e64 v74, v75, v74, s[2:3]
	s_nop 1
	v_add_f32_dpp v74, v74, v74 quad_perm:[2,3,0,1] row_mask:0xf bank_mask:0xf bound_ctrl:1
	s_nop 1
	v_add_f32_dpp v74, v74, v74 quad_perm:[1,0,3,2] row_mask:0xf bank_mask:0xf bound_ctrl:1
	v_cndmask_b32_e64 v74, v113, v74, s[0:1]
	s_and_saveexec_b64 s[0:1], vcc
	ds_write_b32 v114, v74
	s_or_b64 exec, exec, s[0:1]
	v_mov_b32_dpp v90, v74 row_ror:8 row_mask:0xf bank_mask:0xf bound_ctrl:1
	v_add_u32_e32 v114, 32, v114
	v_max_f32_e32 v90, v74, v90
	v_mov_b32_e32 v91, v90
	s_nop 1
	v_permlane16_swap_b32_e32 v90, v91
	s_nop 0
	v_max_f32_e32 v90, v90, v91
	v_mov_b32_e32 v91, v90
	s_nop 1
	v_permlane32_swap_b32_e32 v90, v91
	s_nop 0
	v_max3_f32 v92, v104, v90, v91
	v_sub_f32_e32 v93, v104, v92
	v_sub_f32_e32 v94, v74, v92
	v_exp_f32_e32 v93, v93
	v_exp_f32_e32 v94, v94
	v_mov_b32_e32 v104, v92
	s_nop 1
	v_fma_f32 v105, v105, v93, v94
	s_nop 0
	v_readlane_b32 s34, v93, 0
	v_readlane_b32 s36, v93, 4
	v_readlane_b32 s38, v94, 0
	v_readlane_b32 s40, v94, 4
	v_readlane_b32 s42, v94, 8
	v_readlane_b32 s44, v94, 12
	v_readlane_b32 s46, v94, 16
	v_readlane_b32 s48, v94, 20
	v_readlane_b32 s50, v94, 24
	v_readlane_b32 s52, v94, 28
	v_readlane_b32 s54, v94, 32
	v_readlane_b32 s56, v94, 36
	v_readlane_b32 s58, v94, 40
	v_readlane_b32 s60, v94, 44
	v_readlane_b32 s62, v94, 48
	v_readlane_b32 s64, v94, 52
	v_readlane_b32 s66, v94, 56
	v_readlane_b32 s68, v94, 60
	s_nop 1
	v_pk_mul_f32 v[96:97], v[96:97], s[34:35] op_sel_hi:[1,0]
	v_pk_mul_f32 v[98:99], v[98:99], s[34:35] op_sel_hi:[1,0]
	v_pk_mul_f32 v[100:101], v[100:101], s[36:37] op_sel_hi:[1,0]
	v_pk_mul_f32 v[102:103], v[102:103], s[36:37] op_sel_hi:[1,0]
	v_pk_fma_f32 v[96:97], v[70:71], s[38:39], v[96:97] op_sel_hi:[1,0,1]
	v_pk_fma_f32 v[98:99], v[72:73], s[38:39], v[98:99] op_sel_hi:[1,0,1]
	v_pk_fma_f32 v[100:101], v[70:71], s[40:41], v[100:101] op_sel_hi:[1,0,1]
	v_pk_fma_f32 v[102:103], v[72:73], s[40:41], v[102:103] op_sel_hi:[1,0,1]
	v_pk_fma_f32 v[96:97], v[66:67], s[42:43], v[96:97] op_sel_hi:[1,0,1]
	v_pk_fma_f32 v[98:99], v[68:69], s[42:43], v[98:99] op_sel_hi:[1,0,1]
	v_pk_fma_f32 v[100:101], v[66:67], s[44:45], v[100:101] op_sel_hi:[1,0,1]
	v_pk_fma_f32 v[102:103], v[68:69], s[44:45], v[102:103] op_sel_hi:[1,0,1]
	v_pk_fma_f32 v[96:97], v[62:63], s[46:47], v[96:97] op_sel_hi:[1,0,1]
	v_pk_fma_f32 v[98:99], v[64:65], s[46:47], v[98:99] op_sel_hi:[1,0,1]
	v_pk_fma_f32 v[100:101], v[62:63], s[48:49], v[100:101] op_sel_hi:[1,0,1]
	v_pk_fma_f32 v[102:103], v[64:65], s[48:49], v[102:103] op_sel_hi:[1,0,1]
	v_pk_fma_f32 v[96:97], v[58:59], s[50:51], v[96:97] op_sel_hi:[1,0,1]
	v_pk_fma_f32 v[98:99], v[60:61], s[50:51], v[98:99] op_sel_hi:[1,0,1]
	v_pk_fma_f32 v[100:101], v[58:59], s[52:53], v[100:101] op_sel_hi:[1,0,1]
	v_pk_fma_f32 v[102:103], v[60:61], s[52:53], v[102:103] op_sel_hi:[1,0,1]
	v_pk_fma_f32 v[96:97], v[54:55], s[54:55], v[96:97] op_sel_hi:[1,0,1]
	v_pk_fma_f32 v[98:99], v[56:57], s[54:55], v[98:99] op_sel_hi:[1,0,1]
	v_pk_fma_f32 v[100:101], v[54:55], s[56:57], v[100:101] op_sel_hi:[1,0,1]
	v_pk_fma_f32 v[102:103], v[56:57], s[56:57], v[102:103] op_sel_hi:[1,0,1]
	v_pk_fma_f32 v[96:97], v[46:47], s[58:59], v[96:97] op_sel_hi:[1,0,1]
	v_pk_fma_f32 v[98:99], v[48:49], s[58:59], v[98:99] op_sel_hi:[1,0,1]
	v_pk_fma_f32 v[100:101], v[46:47], s[60:61], v[100:101] op_sel_hi:[1,0,1]
	v_pk_fma_f32 v[102:103], v[48:49], s[60:61], v[102:103] op_sel_hi:[1,0,1]
	v_pk_fma_f32 v[96:97], v[34:35], s[62:63], v[96:97] op_sel_hi:[1,0,1]
	v_pk_fma_f32 v[98:99], v[36:37], s[62:63], v[98:99] op_sel_hi:[1,0,1]
	v_pk_fma_f32 v[100:101], v[34:35], s[64:65], v[100:101] op_sel_hi:[1,0,1]
	v_pk_fma_f32 v[102:103], v[36:37], s[64:65], v[102:103] op_sel_hi:[1,0,1]
	v_pk_fma_f32 v[96:97], v[14:15], s[66:67], v[96:97] op_sel_hi:[1,0,1]
	v_pk_fma_f32 v[98:99], v[16:17], s[66:67], v[98:99] op_sel_hi:[1,0,1]
	v_pk_fma_f32 v[100:101], v[14:15], s[68:69], v[100:101] op_sel_hi:[1,0,1]
	v_pk_fma_f32 v[102:103], v[16:17], s[68:69], v[102:103] op_sel_hi:[1,0,1]
	s_cmp_gt_u32 s30, 20
	s_cbranch_scc1 .Lring_noload_0
	global_load_dword v107, v[118:119], off nt
	global_load_dwordx4 v[70:73], v[116:117], off nt
	global_load_dwordx4 v[66:69], v[116:117], off offset:512 nt
	global_load_dwordx4 v[62:65], v[116:117], off offset:1024 nt
	global_load_dwordx4 v[58:61], v[116:117], off offset:1536 nt
	global_load_dwordx4 v[54:57], v[116:117], off offset:2048 nt
	global_load_dwordx4 v[46:49], v[116:117], off offset:2560 nt
	global_load_dwordx4 v[34:37], v[116:117], off offset:3072 nt
	global_load_dwordx4 v[14:17], v[116:117], off offset:3584 nt
	v_lshl_add_u64 v[116:117], v[116:117], 0, s[16:17]
	v_lshl_add_u64 v[118:119], v[118:119], 0, 32

.Lring_go_1:
	v_mul_f32_e32 v74, v10, v220
	v_mul_f32_e32 v75, v6, v220
	v_mul_f32_e32 v76, v10, v224
	v_mul_f32_e32 v77, v6, v224
	v_mul_f32_e32 v78, v10, v228
	v_mul_f32_e32 v79, v6, v228
	v_mul_f32_e32 v80, v10, v232
	v_mul_f32_e32 v81, v6, v232
	v_mul_f32_e32 v82, v10, v236
	v_mul_f32_e32 v83, v6, v236
	v_mul_f32_e32 v84, v10, v240
	v_mul_f32_e32 v85, v6, v240
	v_mul_f32_e32 v86, v10, v244
	v_mul_f32_e32 v87, v6, v244
	v_mul_f32_e32 v88, v10, v248
	v_mul_f32_e32 v89, v6, v248
	v_fmac_f32_e32 v74, v221, v11
	v_fmac_f32_e32 v75, v221, v7
	v_fmac_f32_e32 v76, v225, v11
	v_fmac_f32_e32 v77, v225, v7
	v_fmac_f32_e32 v78, v229, v11
	v_fmac_f32_e32 v79, v229, v7
	v_fmac_f32_e32 v80, v233, v11
	v_fmac_f32_e32 v81, v233, v7
	v_fmac_f32_e32 v82, v237, v11
	v_fmac_f32_e32 v83, v237, v7
	v_fmac_f32_e32 v84, v241, v11
	v_fmac_f32_e32 v85, v241, v7
	v_fmac_f32_e32 v86, v245, v11
	v_fmac_f32_e32 v87, v245, v7
	v_fmac_f32_e32 v88, v249, v11
	v_fmac_f32_e32 v89, v249, v7
	v_fmac_f32_e32 v74, v222, v12
	v_fmac_f32_e32 v75, v222, v8
	v_fmac_f32_e32 v76, v226, v12
	v_fmac_f32_e32 v77, v226, v8
	v_fmac_f32_e32 v78, v230, v12
	v_fmac_f32_e32 v79, v230, v8
	v_fmac_f32_e32 v80, v234, v12
	v_fmac_f32_e32 v81, v234, v8
	v_fmac_f32_e32 v82, v238, v12
	v_fmac_f32_e32 v83, v238, v8
	v_fmac_f32_e32 v84, v242, v12
	v_fmac_f32_e32 v85, v242, v8
	v_fmac_f32_e32 v86, v246, v12
	v_fmac_f32_e32 v87, v246, v8
	v_fmac_f32_e32 v88, v250, v12
	v_fmac_f32_e32 v89, v250, v8
	v_fmac_f32_e32 v74, v223, v13
	v_fmac_f32_e32 v75, v223, v9
	v_fmac_f32_e32 v76, v227, v13
	v_fmac_f32_e32 v77, v227, v9
	v_fmac_f32_e32 v78, v231, v13
	v_fmac_f32_e32 v79, v231, v9
	v_fmac_f32_e32 v80, v235, v13
	v_fmac_f32_e32 v81, v235, v9
	v_fmac_f32_e32 v82, v239, v13
	v_fmac_f32_e32 v83, v239, v9
	v_fmac_f32_e32 v84, v243, v13
	v_fmac_f32_e32 v85, v243, v9
	v_fmac_f32_e32 v86, v247, v13
	v_fmac_f32_e32 v87, v247, v9
	v_fmac_f32_e32 v88, v251, v13
	v_fmac_f32_e32 v89, v251, v9
	v_permlane32_swap_b32_e32 v74, v82
	v_permlane32_swap_b32_e32 v75, v83
	v_permlane32_swap_b32_e32 v76, v84
	v_permlane32_swap_b32_e32 v77, v85
	v_permlane32_swap_b32_e32 v78, v86
	v_permlane32_swap_b32_e32 v79, v87
	v_permlane32_swap_b32_e32 v80, v88
	v_permlane32_swap_b32_e32 v81, v89
	v_add_f32_e32 v74, v74, v82
	v_add_f32_e32 v75, v75, v83
	v_add_f32_e32 v76, v76, v84
	v_add_f32_e32 v77, v77, v85
	v_add_f32_e32 v78, v78, v86
	v_add_f32_e32 v79, v79, v87
	v_add_f32_e32 v80, v80, v88
	v_add_f32_e32 v81, v81, v89
	v_permlane16_swap_b32_e32 v74, v78
	v_permlane16_swap_b32_e32 v75, v79
	v_permlane16_swap_b32_e32 v76, v80
	v_permlane16_swap_b32_e32 v77, v81
	v_add_f32_e32 v74, v74, v78
	v_add_f32_e32 v75, v75, v79
	v_add_f32_e32 v76, v76, v80
	v_add_f32_e32 v77, v77, v81
	v_add_f32_dpp v74, v74, v74 row_ror:8 row_mask:0xf bank_mask:0xf bound_ctrl:1
	v_add_f32_dpp v76, v76, v76 row_ror:8 row_mask:0xf bank_mask:0xf bound_ctrl:1
	v_add_f32_dpp v75, v75, v75 row_ror:8 row_mask:0xf bank_mask:0xf bound_ctrl:1
	v_add_f32_dpp v77, v77, v77 row_ror:8 row_mask:0xf bank_mask:0xf bound_ctrl:1
	v_cndmask_b32_e64 v74, v76, v74, s[4:5]
	v_cndmask_b32_e64 v75, v77, v75, s[4:5]
	v_cmp_eq_u32_e64 s[0:1], 0, v151
	v_add_f32_dpp v74, v74, v74 row_half_mirror row_mask:0xf bank_mask:0xf bound_ctrl:1
	v_add_f32_dpp v75, v75, v75 row_half_mirror row_mask:0xf bank_mask:0xf bound_ctrl:1
	v_cndmask_b32_e64 v74, v75, v74, s[2:3]
	s_nop 1
	v_add_f32_dpp v74, v74, v74 quad_perm:[2,3,0,1] row_mask:0xf bank_mask:0xf bound_ctrl:1
	s_nop 1
	v_add_f32_dpp v74, v74, v74 quad_perm:[1,0,3,2] row_mask:0xf bank_mask:0xf bound_ctrl:1
	v_cndmask_b32_e64 v74, v113, v74, s[0:1]
	s_and_saveexec_b64 s[0:1], vcc
	ds_write_b32 v114, v74
	s_or_b64 exec, exec, s[0:1]
	v_mov_b32_dpp v90, v74 row_ror:8 row_mask:0xf bank_mask:0xf bound_ctrl:1
	v_add_u32_e32 v114, 32, v114
	v_max_f32_e32 v90, v74, v90
	v_mov_b32_e32 v91, v90
	s_nop 1
	v_permlane16_swap_b32_e32 v90, v91
	s_nop 0
	v_max_f32_e32 v90, v90, v91
	v_mov_b32_e32 v91, v90
	s_nop 1
	v_permlane32_swap_b32_e32 v90, v91
	s_nop 0
	v_max3_f32 v92, v104, v90, v91
	v_sub_f32_e32 v93, v104, v92
	v_sub_f32_e32 v94, v74, v92
	v_exp_f32_e32 v93, v93
	v_exp_f32_e32 v94, v94
	v_mov_b32_e32 v104, v92
	s_nop 1
	v_fma_f32 v105, v105, v93, v94
	s_nop 0
	v_readlane_b32 s34, v93, 0
	v_readlane_b32 s36, v93, 4
	v_readlane_b32 s38, v94, 0
	v_readlane_b32 s40, v94, 4
	v_readlane_b32 s42, v94, 8
	v_readlane_b32 s44, v94, 12
	v_readlane_b32 s46, v94, 16
	v_readlane_b32 s48, v94, 20
	v_readlane_b32 s50, v94, 24
	v_readlane_b32 s52, v94, 28
	v_readlane_b32 s54, v94, 32
	v_readlane_b32 s56, v94, 36
	v_readlane_b32 s58, v94, 40
	v_readlane_b32 s60, v94, 44
	v_readlane_b32 s62, v94, 48
	v_readlane_b32 s64, v94, 52
	v_readlane_b32 s66, v94, 56
	v_readlane_b32 s68, v94, 60
	s_nop 1
	v_pk_mul_f32 v[96:97], v[96:97], s[34:35] op_sel_hi:[1,0]
	v_pk_mul_f32 v[98:99], v[98:99], s[34:35] op_sel_hi:[1,0]
	v_pk_mul_f32 v[100:101], v[100:101], s[36:37] op_sel_hi:[1,0]
	v_pk_mul_f32 v[102:103], v[102:103], s[36:37] op_sel_hi:[1,0]
	v_pk_fma_f32 v[96:97], v[220:221], s[38:39], v[96:97] op_sel_hi:[1,0,1]
	v_pk_fma_f32 v[98:99], v[222:223], s[38:39], v[98:99] op_sel_hi:[1,0,1]
	v_pk_fma_f32 v[100:101], v[220:221], s[40:41], v[100:101] op_sel_hi:[1,0,1]
	v_pk_fma_f32 v[102:103], v[222:223], s[40:41], v[102:103] op_sel_hi:[1,0,1]
	v_pk_fma_f32 v[96:97], v[224:225], s[42:43], v[96:97] op_sel_hi:[1,0,1]
	v_pk_fma_f32 v[98:99], v[226:227], s[42:43], v[98:99] op_sel_hi:[1,0,1]
	v_pk_fma_f32 v[100:101], v[224:225], s[44:45], v[100:101] op_sel_hi:[1,0,1]
	v_pk_fma_f32 v[102:103], v[226:227], s[44:45], v[102:103] op_sel_hi:[1,0,1]
	v_pk_fma_f32 v[96:97], v[228:229], s[46:47], v[96:97] op_sel_hi:[1,0,1]
	v_pk_fma_f32 v[98:99], v[230:231], s[46:47], v[98:99] op_sel_hi:[1,0,1]
	v_pk_fma_f32 v[100:101], v[228:229], s[48:49], v[100:101] op_sel_hi:[1,0,1]
	v_pk_fma_f32 v[102:103], v[230:231], s[48:49], v[102:103] op_sel_hi:[1,0,1]
	v_pk_fma_f32 v[96:97], v[232:233], s[50:51], v[96:97] op_sel_hi:[1,0,1]
	v_pk_fma_f32 v[98:99], v[234:235], s[50:51], v[98:99] op_sel_hi:[1,0,1]
	v_pk_fma_f32 v[100:101], v[232:233], s[52:53], v[100:101] op_sel_hi:[1,0,1]
	v_pk_fma_f32 v[102:103], v[234:235], s[52:53], v[102:103] op_sel_hi:[1,0,1]
	v_pk_fma_f32 v[96:97], v[236:237], s[54:55], v[96:97] op_sel_hi:[1,0,1]
	v_pk_fma_f32 v[98:99], v[238:239], s[54:55], v[98:99] op_sel_hi:[1,0,1]
	v_pk_fma_f32 v[100:101], v[236:237], s[56:57], v[100:101] op_sel_hi:[1,0,1]
	v_pk_fma_f32 v[102:103], v[238:239], s[56:57], v[102:103] op_sel_hi:[1,0,1]
	v_pk_fma_f32 v[96:97], v[240:241], s[58:59], v[96:97] op_sel_hi:[1,0,1]
	v_pk_fma_f32 v[98:99], v[242:243], s[58:59], v[98:99] op_sel_hi:[1,0,1]
	v_pk_fma_f32 v[100:101], v[240:241], s[60:61], v[100:101] op_sel_hi:[1,0,1]
	v_pk_fma_f32 v[102:103], v[242:243], s[60:61], v[102:103] op_sel_hi:[1,0,1]
	v_pk_fma_f32 v[96:97], v[244:245], s[62:63], v[96:97] op_sel_hi:[1,0,1]
	v_pk_fma_f32 v[98:99], v[246:247], s[62:63], v[98:99] op_sel_hi:[1,0,1]
	v_pk_fma_f32 v[100:101], v[244:245], s[64:65], v[100:101] op_sel_hi:[1,0,1]
	v_pk_fma_f32 v[102:103], v[246:247], s[64:65], v[102:103] op_sel_hi:[1,0,1]
	v_pk_fma_f32 v[96:97], v[248:249], s[66:67], v[96:97] op_sel_hi:[1,0,1]
	v_pk_fma_f32 v[98:99], v[250:251], s[66:67], v[98:99] op_sel_hi:[1,0,1]
	v_pk_fma_f32 v[100:101], v[248:249], s[68:69], v[100:101] op_sel_hi:[1,0,1]
	v_pk_fma_f32 v[102:103], v[250:251], s[68:69], v[102:103] op_sel_hi:[1,0,1]
	s_cmp_gt_u32 s30, 20
	s_cbranch_scc1 .Lring_noload_1
	global_load_dword v151, v[118:119], off nt
	global_load_dwordx4 v[220:223], v[116:117], off nt
	global_load_dwordx4 v[224:227], v[116:117], off offset:512 nt
	global_load_dwordx4 v[228:231], v[116:117], off offset:1024 nt
	global_load_dwordx4 v[232:235], v[116:117], off offset:1536 nt
	global_load_dwordx4 v[236:239], v[116:117], off offset:2048 nt
	global_load_dwordx4 v[240:243], v[116:117], off offset:2560 nt
	global_load_dwordx4 v[244:247], v[116:117], off offset:3072 nt
	global_load_dwordx4 v[248:251], v[116:117], off offset:3584 nt
	v_lshl_add_u64 v[116:117], v[116:117], 0, s[16:17]
	v_lshl_add_u64 v[118:119], v[118:119], 0, 32

.Lring_go_2:
	v_mul_f32_e32 v74, v10, v50
	v_mul_f32_e32 v75, v6, v50
	v_mul_f32_e32 v76, v10, v42
	v_mul_f32_e32 v77, v6, v42
	v_mul_f32_e32 v78, v10, v38
	v_mul_f32_e32 v79, v6, v38
	v_mul_f32_e32 v80, v10, v30
	v_mul_f32_e32 v81, v6, v30
	v_mul_f32_e32 v82, v10, v26
	v_mul_f32_e32 v83, v6, v26
	v_mul_f32_e32 v84, v10, v22
	v_mul_f32_e32 v85, v6, v22
	v_mul_f32_e32 v86, v10, v18
	v_mul_f32_e32 v87, v6, v18
	v_mul_f32_e32 v88, v10, v252
	v_mul_f32_e32 v89, v6, v252
	v_fmac_f32_e32 v74, v51, v11
	v_fmac_f32_e32 v75, v51, v7
	v_fmac_f32_e32 v76, v43, v11
	v_fmac_f32_e32 v77, v43, v7
	v_fmac_f32_e32 v78, v39, v11
	v_fmac_f32_e32 v79, v39, v7
	v_fmac_f32_e32 v80, v31, v11
	v_fmac_f32_e32 v81, v31, v7
	v_fmac_f32_e32 v82, v27, v11
	v_fmac_f32_e32 v83, v27, v7
	v_fmac_f32_e32 v84, v23, v11
	v_fmac_f32_e32 v85, v23, v7
	v_fmac_f32_e32 v86, v19, v11
	v_fmac_f32_e32 v87, v19, v7
	v_fmac_f32_e32 v88, v253, v11
	v_fmac_f32_e32 v89, v253, v7
	v_fmac_f32_e32 v74, v52, v12
	v_fmac_f32_e32 v75, v52, v8
	v_fmac_f32_e32 v76, v44, v12
	v_fmac_f32_e32 v77, v44, v8
	v_fmac_f32_e32 v78, v40, v12
	v_fmac_f32_e32 v79, v40, v8
	v_fmac_f32_e32 v80, v32, v12
	v_fmac_f32_e32 v81, v32, v8
	v_fmac_f32_e32 v82, v28, v12
	v_fmac_f32_e32 v83, v28, v8
	v_fmac_f32_e32 v84, v24, v12
	v_fmac_f32_e32 v85, v24, v8
	v_fmac_f32_e32 v86, v20, v12
	v_fmac_f32_e32 v87, v20, v8
	v_fmac_f32_e32 v88, v254, v12
	v_fmac_f32_e32 v89, v254, v8
	v_fmac_f32_e32 v74, v53, v13
	v_fmac_f32_e32 v75, v53, v9
	v_fmac_f32_e32 v76, v45, v13
	v_fmac_f32_e32 v77, v45, v9
	v_fmac_f32_e32 v78, v41, v13
	v_fmac_f32_e32 v79, v41, v9
	v_fmac_f32_e32 v80, v33, v13
	v_fmac_f32_e32 v81, v33, v9
	v_fmac_f32_e32 v82, v29, v13
	v_fmac_f32_e32 v83, v29, v9
	v_fmac_f32_e32 v84, v25, v13
	v_fmac_f32_e32 v85, v25, v9
	v_fmac_f32_e32 v86, v21, v13
	v_fmac_f32_e32 v87, v21, v9
	v_fmac_f32_e32 v88, v255, v13
	v_fmac_f32_e32 v89, v255, v9
	v_permlane32_swap_b32_e32 v74, v82
	v_permlane32_swap_b32_e32 v75, v83
	v_permlane32_swap_b32_e32 v76, v84
	v_permlane32_swap_b32_e32 v77, v85
	v_permlane32_swap_b32_e32 v78, v86
	v_permlane32_swap_b32_e32 v79, v87
	v_permlane32_swap_b32_e32 v80, v88
	v_permlane32_swap_b32_e32 v81, v89
	v_add_f32_e32 v74, v74, v82
	v_add_f32_e32 v75, v75, v83
	v_add_f32_e32 v76, v76, v84
	v_add_f32_e32 v77, v77, v85
	v_add_f32_e32 v78, v78, v86
	v_add_f32_e32 v79, v79, v87
	v_add_f32_e32 v80, v80, v88
	v_add_f32_e32 v81, v81, v89
	v_permlane16_swap_b32_e32 v74, v78
	v_permlane16_swap_b32_e32 v75, v79
	v_permlane16_swap_b32_e32 v76, v80
	v_permlane16_swap_b32_e32 v77, v81
	v_add_f32_e32 v74, v74, v78
	v_add_f32_e32 v75, v75, v79
	v_add_f32_e32 v76, v76, v80
	v_add_f32_e32 v77, v77, v81
	v_add_f32_dpp v74, v74, v74 row_ror:8 row_mask:0xf bank_mask:0xf bound_ctrl:1
	v_add_f32_dpp v76, v76, v76 row_ror:8 row_mask:0xf bank_mask:0xf bound_ctrl:1
	v_add_f32_dpp v75, v75, v75 row_ror:8 row_mask:0xf bank_mask:0xf bound_ctrl:1
	v_add_f32_dpp v77, v77, v77 row_ror:8 row_mask:0xf bank_mask:0xf bound_ctrl:1
	v_cndmask_b32_e64 v74, v76, v74, s[4:5]
	v_cndmask_b32_e64 v75, v77, v75, s[4:5]
	v_cmp_eq_u32_e64 s[0:1], 0, v193
	v_add_f32_dpp v74, v74, v74 row_half_mirror row_mask:0xf bank_mask:0xf bound_ctrl:1
	v_add_f32_dpp v75, v75, v75 row_half_mirror row_mask:0xf bank_mask:0xf bound_ctrl:1
	v_cndmask_b32_e64 v74, v75, v74, s[2:3]
	s_nop 1
	v_add_f32_dpp v74, v74, v74 quad_perm:[2,3,0,1] row_mask:0xf bank_mask:0xf bound_ctrl:1
	s_nop 1
	v_add_f32_dpp v74, v74, v74 quad_perm:[1,0,3,2] row_mask:0xf bank_mask:0xf bound_ctrl:1
	v_cndmask_b32_e64 v74, v113, v74, s[0:1]
	s_and_saveexec_b64 s[0:1], vcc
	ds_write_b32 v114, v74
	s_or_b64 exec, exec, s[0:1]
	v_mov_b32_dpp v90, v74 row_ror:8 row_mask:0xf bank_mask:0xf bound_ctrl:1
	v_add_u32_e32 v114, 32, v114
	v_max_f32_e32 v90, v74, v90
	v_mov_b32_e32 v91, v90
	s_nop 1
	v_permlane16_swap_b32_e32 v90, v91
	s_nop 0
	v_max_f32_e32 v90, v90, v91
	v_mov_b32_e32 v91, v90
	s_nop 1
	v_permlane32_swap_b32_e32 v90, v91
	s_nop 0
	v_max3_f32 v92, v104, v90, v91
	v_sub_f32_e32 v93, v104, v92
	v_sub_f32_e32 v94, v74, v92
	v_exp_f32_e32 v93, v93
	v_exp_f32_e32 v94, v94
	v_mov_b32_e32 v104, v92
	s_nop 1
	v_fma_f32 v105, v105, v93, v94
	s_nop 0
	v_readlane_b32 s34, v93, 0
	v_readlane_b32 s36, v93, 4
	v_readlane_b32 s38, v94, 0
	v_readlane_b32 s40, v94, 4
	v_readlane_b32 s42, v94, 8
	v_readlane_b32 s44, v94, 12
	v_readlane_b32 s46, v94, 16
	v_readlane_b32 s48, v94, 20
	v_readlane_b32 s50, v94, 24
	v_readlane_b32 s52, v94, 28
	v_readlane_b32 s54, v94, 32
	v_readlane_b32 s56, v94, 36
	v_readlane_b32 s58, v94, 40
	v_readlane_b32 s60, v94, 44
	v_readlane_b32 s62, v94, 48
	v_readlane_b32 s64, v94, 52
	v_readlane_b32 s66, v94, 56
	v_readlane_b32 s68, v94, 60
	s_nop 1
	v_pk_mul_f32 v[96:97], v[96:97], s[34:35] op_sel_hi:[1,0]
	v_pk_mul_f32 v[98:99], v[98:99], s[34:35] op_sel_hi:[1,0]
	v_pk_mul_f32 v[100:101], v[100:101], s[36:37] op_sel_hi:[1,0]
	v_pk_mul_f32 v[102:103], v[102:103], s[36:37] op_sel_hi:[1,0]
	v_pk_fma_f32 v[96:97], v[50:51], s[38:39], v[96:97] op_sel_hi:[1,0,1]
	v_pk_fma_f32 v[98:99], v[52:53], s[38:39], v[98:99] op_sel_hi:[1,0,1]
	v_pk_fma_f32 v[100:101], v[50:51], s[40:41], v[100:101] op_sel_hi:[1,0,1]
	v_pk_fma_f32 v[102:103], v[52:53], s[40:41], v[102:103] op_sel_hi:[1,0,1]
	v_pk_fma_f32 v[96:97], v[42:43], s[42:43], v[96:97] op_sel_hi:[1,0,1]
	v_pk_fma_f32 v[98:99], v[44:45], s[42:43], v[98:99] op_sel_hi:[1,0,1]
	v_pk_fma_f32 v[100:101], v[42:43], s[44:45], v[100:101] op_sel_hi:[1,0,1]
	v_pk_fma_f32 v[102:103], v[44:45], s[44:45], v[102:103] op_sel_hi:[1,0,1]
	v_pk_fma_f32 v[96:97], v[38:39], s[46:47], v[96:97] op_sel_hi:[1,0,1]
	v_pk_fma_f32 v[98:99], v[40:41], s[46:47], v[98:99] op_sel_hi:[1,0,1]
	v_pk_fma_f32 v[100:101], v[38:39], s[48:49], v[100:101] op_sel_hi:[1,0,1]
	v_pk_fma_f32 v[102:103], v[40:41], s[48:49], v[102:103] op_sel_hi:[1,0,1]
	v_pk_fma_f32 v[96:97], v[30:31], s[50:51], v[96:97] op_sel_hi:[1,0,1]
	v_pk_fma_f32 v[98:99], v[32:33], s[50:51], v[98:99] op_sel_hi:[1,0,1]
	v_pk_fma_f32 v[100:101], v[30:31], s[52:53], v[100:101] op_sel_hi:[1,0,1]
	v_pk_fma_f32 v[102:103], v[32:33], s[52:53], v[102:103] op_sel_hi:[1,0,1]
	v_pk_fma_f32 v[96:97], v[26:27], s[54:55], v[96:97] op_sel_hi:[1,0,1]
	v_pk_fma_f32 v[98:99], v[28:29], s[54:55], v[98:99] op_sel_hi:[1,0,1]
	v_pk_fma_f32 v[100:101], v[26:27], s[56:57], v[100:101] op_sel_hi:[1,0,1]
	v_pk_fma_f32 v[102:103], v[28:29], s[56:57], v[102:103] op_sel_hi:[1,0,1]
	v_pk_fma_f32 v[96:97], v[22:23], s[58:59], v[96:97] op_sel_hi:[1,0,1]
	v_pk_fma_f32 v[98:99], v[24:25], s[58:59], v[98:99] op_sel_hi:[1,0,1]
	v_pk_fma_f32 v[100:101], v[22:23], s[60:61], v[100:101] op_sel_hi:[1,0,1]
	v_pk_fma_f32 v[102:103], v[24:25], s[60:61], v[102:103] op_sel_hi:[1,0,1]
	v_pk_fma_f32 v[96:97], v[18:19], s[62:63], v[96:97] op_sel_hi:[1,0,1]
	v_pk_fma_f32 v[98:99], v[20:21], s[62:63], v[98:99] op_sel_hi:[1,0,1]
	v_pk_fma_f32 v[100:101], v[18:19], s[64:65], v[100:101] op_sel_hi:[1,0,1]
	v_pk_fma_f32 v[102:103], v[20:21], s[64:65], v[102:103] op_sel_hi:[1,0,1]
	v_pk_fma_f32 v[96:97], v[252:253], s[66:67], v[96:97] op_sel_hi:[1,0,1]
	v_pk_fma_f32 v[98:99], v[254:255], s[66:67], v[98:99] op_sel_hi:[1,0,1]
	v_pk_fma_f32 v[100:101], v[252:253], s[68:69], v[100:101] op_sel_hi:[1,0,1]
	v_pk_fma_f32 v[102:103], v[254:255], s[68:69], v[102:103] op_sel_hi:[1,0,1]
	s_cmp_gt_u32 s30, 20
	s_cbranch_scc1 .Lring_noload_2
	global_load_dword v193, v[118:119], off nt
	global_load_dwordx4 v[50:53], v[116:117], off nt
	global_load_dwordx4 v[42:45], v[116:117], off offset:512 nt
	global_load_dwordx4 v[38:41], v[116:117], off offset:1024 nt
	global_load_dwordx4 v[30:33], v[116:117], off offset:1536 nt
	global_load_dwordx4 v[26:29], v[116:117], off offset:2048 nt
	global_load_dwordx4 v[22:25], v[116:117], off offset:2560 nt
	global_load_dwordx4 v[18:21], v[116:117], off offset:3072 nt
	global_load_dwordx4 v[252:255], v[116:117], off offset:3584 nt
	v_lshl_add_u64 v[116:117], v[116:117], 0, s[16:17]
	v_lshl_add_u64 v[118:119], v[118:119], 0, 32

.Lring_go_3:
	v_mul_f32_e32 v74, v10, v138
	v_mul_f32_e32 v75, v6, v138
	v_mul_f32_e32 v76, v10, v146
	v_mul_f32_e32 v77, v6, v146
	v_mul_f32_e32 v78, v10, v152
	v_mul_f32_e32 v79, v6, v152
	v_mul_f32_e32 v80, v10, v156
	v_mul_f32_e32 v81, v6, v156
	v_mul_f32_e32 v82, v10, v160
	v_mul_f32_e32 v83, v6, v160
	v_mul_f32_e32 v84, v10, v164
	v_mul_f32_e32 v85, v6, v164
	v_mul_f32_e32 v86, v10, v168
	v_mul_f32_e32 v87, v6, v168
	v_mul_f32_e32 v88, v10, v172
	v_mul_f32_e32 v89, v6, v172
	v_fmac_f32_e32 v74, v139, v11
	v_fmac_f32_e32 v75, v139, v7
	v_fmac_f32_e32 v76, v147, v11
	v_fmac_f32_e32 v77, v147, v7
	v_fmac_f32_e32 v78, v153, v11
	v_fmac_f32_e32 v79, v153, v7
	v_fmac_f32_e32 v80, v157, v11
	v_fmac_f32_e32 v81, v157, v7
	v_fmac_f32_e32 v82, v161, v11
	v_fmac_f32_e32 v83, v161, v7
	v_fmac_f32_e32 v84, v165, v11
	v_fmac_f32_e32 v85, v165, v7
	v_fmac_f32_e32 v86, v169, v11
	v_fmac_f32_e32 v87, v169, v7
	v_fmac_f32_e32 v88, v173, v11
	v_fmac_f32_e32 v89, v173, v7
	v_fmac_f32_e32 v74, v140, v12
	v_fmac_f32_e32 v75, v140, v8
	v_fmac_f32_e32 v76, v148, v12
	v_fmac_f32_e32 v77, v148, v8
	v_fmac_f32_e32 v78, v154, v12
	v_fmac_f32_e32 v79, v154, v8
	v_fmac_f32_e32 v80, v158, v12
	v_fmac_f32_e32 v81, v158, v8
	v_fmac_f32_e32 v82, v162, v12
	v_fmac_f32_e32 v83, v162, v8
	v_fmac_f32_e32 v84, v166, v12
	v_fmac_f32_e32 v85, v166, v8
	v_fmac_f32_e32 v86, v170, v12
	v_fmac_f32_e32 v87, v170, v8
	v_fmac_f32_e32 v88, v174, v12
	v_fmac_f32_e32 v89, v174, v8
	v_fmac_f32_e32 v74, v141, v13
	v_fmac_f32_e32 v75, v141, v9
	v_fmac_f32_e32 v76, v149, v13
	v_fmac_f32_e32 v77, v149, v9
	v_fmac_f32_e32 v78, v155, v13
	v_fmac_f32_e32 v79, v155, v9
	v_fmac_f32_e32 v80, v159, v13
	v_fmac_f32_e32 v81, v159, v9
	v_fmac_f32_e32 v82, v163, v13
	v_fmac_f32_e32 v83, v163, v9
	v_fmac_f32_e32 v84, v167, v13
	v_fmac_f32_e32 v85, v167, v9
	v_fmac_f32_e32 v86, v171, v13
	v_fmac_f32_e32 v87, v171, v9
	v_fmac_f32_e32 v88, v175, v13
	v_fmac_f32_e32 v89, v175, v9
	v_permlane32_swap_b32_e32 v74, v82
	v_permlane32_swap_b32_e32 v75, v83
	v_permlane32_swap_b32_e32 v76, v84
	v_permlane32_swap_b32_e32 v77, v85
	v_permlane32_swap_b32_e32 v78, v86
	v_permlane32_swap_b32_e32 v79, v87
	v_permlane32_swap_b32_e32 v80, v88
	v_permlane32_swap_b32_e32 v81, v89
	v_add_f32_e32 v74, v74, v82
	v_add_f32_e32 v75, v75, v83
	v_add_f32_e32 v76, v76, v84
	v_add_f32_e32 v77, v77, v85
	v_add_f32_e32 v78, v78, v86
	v_add_f32_e32 v79, v79, v87
	v_add_f32_e32 v80, v80, v88
	v_add_f32_e32 v81, v81, v89
	v_permlane16_swap_b32_e32 v74, v78
	v_permlane16_swap_b32_e32 v75, v79
	v_permlane16_swap_b32_e32 v76, v80
	v_permlane16_swap_b32_e32 v77, v81
	v_add_f32_e32 v74, v74, v78
	v_add_f32_e32 v75, v75, v79
	v_add_f32_e32 v76, v76, v80
	v_add_f32_e32 v77, v77, v81
	v_add_f32_dpp v74, v74, v74 row_ror:8 row_mask:0xf bank_mask:0xf bound_ctrl:1
	v_add_f32_dpp v76, v76, v76 row_ror:8 row_mask:0xf bank_mask:0xf bound_ctrl:1
	v_add_f32_dpp v75, v75, v75 row_ror:8 row_mask:0xf bank_mask:0xf bound_ctrl:1
	v_add_f32_dpp v77, v77, v77 row_ror:8 row_mask:0xf bank_mask:0xf bound_ctrl:1
	v_cndmask_b32_e64 v74, v76, v74, s[4:5]
	v_cndmask_b32_e64 v75, v77, v75, s[4:5]
	v_cmp_eq_u32_e64 s[0:1], 0, v205
	v_add_f32_dpp v74, v74, v74 row_half_mirror row_mask:0xf bank_mask:0xf bound_ctrl:1
	v_add_f32_dpp v75, v75, v75 row_half_mirror row_mask:0xf bank_mask:0xf bound_ctrl:1
	v_cndmask_b32_e64 v74, v75, v74, s[2:3]
	s_nop 1
	v_add_f32_dpp v74, v74, v74 quad_perm:[2,3,0,1] row_mask:0xf bank_mask:0xf bound_ctrl:1
	s_nop 1
	v_add_f32_dpp v74, v74, v74 quad_perm:[1,0,3,2] row_mask:0xf bank_mask:0xf bound_ctrl:1
	v_cndmask_b32_e64 v74, v113, v74, s[0:1]
	s_and_saveexec_b64 s[0:1], vcc
	ds_write_b32 v114, v74
	s_or_b64 exec, exec, s[0:1]
	v_mov_b32_dpp v90, v74 row_ror:8 row_mask:0xf bank_mask:0xf bound_ctrl:1
	v_add_u32_e32 v114, 32, v114
	v_max_f32_e32 v90, v74, v90
	v_mov_b32_e32 v91, v90
	s_nop 1
	v_permlane16_swap_b32_e32 v90, v91
	s_nop 0
	v_max_f32_e32 v90, v90, v91
	v_mov_b32_e32 v91, v90
	s_nop 1
	v_permlane32_swap_b32_e32 v90, v91
	s_nop 0
	v_max3_f32 v92, v104, v90, v91
	v_sub_f32_e32 v93, v104, v92
	v_sub_f32_e32 v94, v74, v92
	v_exp_f32_e32 v93, v93
	v_exp_f32_e32 v94, v94
	v_mov_b32_e32 v104, v92
	s_nop 1
	v_fma_f32 v105, v105, v93, v94
	s_nop 0
	v_readlane_b32 s34, v93, 0
	v_readlane_b32 s36, v93, 4
	v_readlane_b32 s38, v94, 0
	v_readlane_b32 s40, v94, 4
	v_readlane_b32 s42, v94, 8
	v_readlane_b32 s44, v94, 12
	v_readlane_b32 s46, v94, 16
	v_readlane_b32 s48, v94, 20
	v_readlane_b32 s50, v94, 24
	v_readlane_b32 s52, v94, 28
	v_readlane_b32 s54, v94, 32
	v_readlane_b32 s56, v94, 36
	v_readlane_b32 s58, v94, 40
	v_readlane_b32 s60, v94, 44
	v_readlane_b32 s62, v94, 48
	v_readlane_b32 s64, v94, 52
	v_readlane_b32 s66, v94, 56
	v_readlane_b32 s68, v94, 60
	s_nop 1
	v_pk_mul_f32 v[96:97], v[96:97], s[34:35] op_sel_hi:[1,0]
	v_pk_mul_f32 v[98:99], v[98:99], s[34:35] op_sel_hi:[1,0]
	v_pk_mul_f32 v[100:101], v[100:101], s[36:37] op_sel_hi:[1,0]
	v_pk_mul_f32 v[102:103], v[102:103], s[36:37] op_sel_hi:[1,0]
	v_pk_fma_f32 v[96:97], v[138:139], s[38:39], v[96:97] op_sel_hi:[1,0,1]
	v_pk_fma_f32 v[98:99], v[140:141], s[38:39], v[98:99] op_sel_hi:[1,0,1]
	v_pk_fma_f32 v[100:101], v[138:139], s[40:41], v[100:101] op_sel_hi:[1,0,1]
	v_pk_fma_f32 v[102:103], v[140:141], s[40:41], v[102:103] op_sel_hi:[1,0,1]
	v_pk_fma_f32 v[96:97], v[146:147], s[42:43], v[96:97] op_sel_hi:[1,0,1]
	v_pk_fma_f32 v[98:99], v[148:149], s[42:43], v[98:99] op_sel_hi:[1,0,1]
	v_pk_fma_f32 v[100:101], v[146:147], s[44:45], v[100:101] op_sel_hi:[1,0,1]
	v_pk_fma_f32 v[102:103], v[148:149], s[44:45], v[102:103] op_sel_hi:[1,0,1]
	v_pk_fma_f32 v[96:97], v[152:153], s[46:47], v[96:97] op_sel_hi:[1,0,1]
	v_pk_fma_f32 v[98:99], v[154:155], s[46:47], v[98:99] op_sel_hi:[1,0,1]
	v_pk_fma_f32 v[100:101], v[152:153], s[48:49], v[100:101] op_sel_hi:[1,0,1]
	v_pk_fma_f32 v[102:103], v[154:155], s[48:49], v[102:103] op_sel_hi:[1,0,1]
	v_pk_fma_f32 v[96:97], v[156:157], s[50:51], v[96:97] op_sel_hi:[1,0,1]
	v_pk_fma_f32 v[98:99], v[158:159], s[50:51], v[98:99] op_sel_hi:[1,0,1]
	v_pk_fma_f32 v[100:101], v[156:157], s[52:53], v[100:101] op_sel_hi:[1,0,1]
	v_pk_fma_f32 v[102:103], v[158:159], s[52:53], v[102:103] op_sel_hi:[1,0,1]
	v_pk_fma_f32 v[96:97], v[160:161], s[54:55], v[96:97] op_sel_hi:[1,0,1]
	v_pk_fma_f32 v[98:99], v[162:163], s[54:55], v[98:99] op_sel_hi:[1,0,1]
	v_pk_fma_f32 v[100:101], v[160:161], s[56:57], v[100:101] op_sel_hi:[1,0,1]
	v_pk_fma_f32 v[102:103], v[162:163], s[56:57], v[102:103] op_sel_hi:[1,0,1]
	v_pk_fma_f32 v[96:97], v[164:165], s[58:59], v[96:97] op_sel_hi:[1,0,1]
	v_pk_fma_f32 v[98:99], v[166:167], s[58:59], v[98:99] op_sel_hi:[1,0,1]
	v_pk_fma_f32 v[100:101], v[164:165], s[60:61], v[100:101] op_sel_hi:[1,0,1]
	v_pk_fma_f32 v[102:103], v[166:167], s[60:61], v[102:103] op_sel_hi:[1,0,1]
	v_pk_fma_f32 v[96:97], v[168:169], s[62:63], v[96:97] op_sel_hi:[1,0,1]
	v_pk_fma_f32 v[98:99], v[170:171], s[62:63], v[98:99] op_sel_hi:[1,0,1]
	v_pk_fma_f32 v[100:101], v[168:169], s[64:65], v[100:101] op_sel_hi:[1,0,1]
	v_pk_fma_f32 v[102:103], v[170:171], s[64:65], v[102:103] op_sel_hi:[1,0,1]
	v_pk_fma_f32 v[96:97], v[172:173], s[66:67], v[96:97] op_sel_hi:[1,0,1]
	v_pk_fma_f32 v[98:99], v[174:175], s[66:67], v[98:99] op_sel_hi:[1,0,1]
	v_pk_fma_f32 v[100:101], v[172:173], s[68:69], v[100:101] op_sel_hi:[1,0,1]
	v_pk_fma_f32 v[102:103], v[174:175], s[68:69], v[102:103] op_sel_hi:[1,0,1]
	s_cmp_gt_u32 s30, 20
	s_cbranch_scc1 .Lring_noload_3
	global_load_dword v205, v[118:119], off nt
	global_load_dwordx4 v[138:141], v[116:117], off nt
	global_load_dwordx4 v[146:149], v[116:117], off offset:512 nt
	global_load_dwordx4 v[152:155], v[116:117], off offset:1024 nt
	global_load_dwordx4 v[156:159], v[116:117], off offset:1536 nt
	global_load_dwordx4 v[160:163], v[116:117], off offset:2048 nt
	global_load_dwordx4 v[164:167], v[116:117], off offset:2560 nt
	global_load_dwordx4 v[168:171], v[116:117], off offset:3072 nt
	global_load_dwordx4 v[172:175], v[116:117], off offset:3584 nt
	v_lshl_add_u64 v[116:117], v[116:117], 0, s[16:17]
	v_lshl_add_u64 v[118:119], v[118:119], 0, 32

.Lring_done:
	v_mov_b32_e32 v240, v96
	v_mov_b32_e32 v241, v97
	v_mov_b32_e32 v242, v98
	v_mov_b32_e32 v243, v99
	v_mov_b32_e32 v244, v100
	v_mov_b32_e32 v245, v101
	v_mov_b32_e32 v246, v102
	v_mov_b32_e32 v247, v103
	v_mov_b32_e32 v248, v104
	v_mov_b32_e32 v249, v105
	s_movk_i32 s0, 0x640
	v_mov_b32_e32 v14, 0x8200
	v_mad_u32_u24 v205, v197, s0, v14
	v_lshlrev_b32_e32 v10, 4, v106
	v_or_b32_e32 v6, 0x2000, v196
	v_add_lshl_u32 v7, v122, v6, 4
	global_load_dwordx4 v[158:161], v10, s[8:9]
	global_load_dwordx4 v[154:157], v10, s[8:9] offset:1024
	global_load_dwordx4 v[146:149], v10, s[8:9] offset:2048
	global_load_dwordx4 v[138:141], v10, s[8:9] offset:3072
	global_load_dwordx4 v[118:121], v131, s[8:9]
	global_load_dwordx4 v[106:109], v132, s[8:9]
	global_load_dwordx4 v[98:101], v133, s[8:9]
	global_load_dwordx4 v[102:105], v134, s[8:9]
	global_load_dwordx4 v[170:173], v135, s[8:9]
	global_load_dwordx4 v[166:169], v137, s[8:9]
	global_load_dwordx4 v[178:181], v136, s[8:9]
	global_load_dwordx4 v[174:177], v142, s[8:9]
	global_load_dwordx4 v[162:165], v143, s[8:9]
	s_nop 0
	global_load_dwordx4 v[134:137], v144, s[8:9]
	global_load_dwordx4 v[114:117], v145, s[8:9]
	global_load_dwordx4 v[110:113], v150, s[8:9]
	global_load_dwordx4 v[94:97], v7, s[8:9]
	global_load_dwordx4 v[90:93], v7, s[8:9] offset:1024
	global_load_dwordx4 v[78:81], v7, s[8:9] offset:2048
	global_load_dwordx4 v[74:77], v7, s[8:9] offset:3072
	v_add_lshl_u32 v7, v123, v6, 4
	v_add_lshl_u32 v8, v124, v6, 4
	global_load_dwordx4 v[66:69], v7, s[8:9]
	global_load_dwordx4 v[58:61], v8, s[8:9]
	v_add_lshl_u32 v7, v125, v6, 4
	v_add_lshl_u32 v8, v126, v6, 4
	global_load_dwordx4 v[62:65], v7, s[8:9]
	global_load_dwordx4 v[54:57], v8, s[8:9]
	v_add_lshl_u32 v7, v127, v6, 4
	v_add_lshl_u32 v8, v128, v6, 4
	global_load_dwordx4 v[150:153], v7, s[8:9]
	global_load_dwordx4 v[142:145], v8, s[8:9]
	v_add_lshl_u32 v7, v129, v6, 4
	v_add_lshl_u32 v8, v130, v6, 4
	global_load_dwordx4 v[130:133], v7, s[8:9]
	global_load_dwordx4 v[126:129], v8, s[8:9]
	v_add_lshl_u32 v7, v192, v6, 4
	v_add_lshl_u32 v8, v202, v6, 4
	global_load_dwordx4 v[122:125], v7, s[8:9]
	global_load_dwordx4 v[82:85], v8, s[8:9]
	v_add_lshl_u32 v7, v203, v6, 4
	v_add_lshl_u32 v6, v204, v6, 4
	global_load_dwordx4 v[86:89], v7, s[8:9]
	global_load_dwordx4 v[70:73], v6, s[8:9]
	v_lshlrev_b32_e32 v187, 2, v195
	v_and_or_b32 v190, v187, 4, s31
	v_or_b32_e32 v208, 1, v190
	v_mul_u32_u24_e32 v6, 0x300, v197
	v_ashrrev_i32_e32 v191, 31, v190
	v_ashrrev_i32_e32 v209, 31, v208
	v_or_b32_e32 v6, v196, v6
	v_lshlrev_b64 v[210:211], 9, v[190:191]
	v_lshlrev_b32_e32 v191, 2, v1
	v_lshlrev_b64 v[222:223], 9, v[208:209]
	v_or_b32_e32 v208, 2, v190
	v_mov_b32_e32 v193, 0
	v_lshlrev_b32_e32 v14, 4, v6
	v_lshl_or_b32 v192, v197, 7, v191
	s_movk_i32 s2, 0xfe00
	v_ashrrev_i32_e32 v209, 31, v208
	v_or_b32_e32 v6, 0x40000, v14
	s_movk_i32 s1, 0x100
	v_lshl_add_u64 v[220:221], s[22:23], 0, v[192:193]
	s_mov_b32 s3, -1
	v_lshlrev_b64 v[226:227], 9, v[208:209]
	v_or_b32_e32 v208, 3, v190
	global_load_dwordx4 v[50:53], v6, s[8:9]
	global_load_dwordx4 v[46:49], v6, s[8:9] offset:1024
	global_load_dwordx4 v[42:45], v6, s[8:9] offset:2048
	global_load_dwordx4 v[30:33], v6, s[8:9] offset:3072
	v_add_u32_e32 v6, 0x41000, v14
	v_add_u32_e32 v7, 0x41400, v14
	v_lshl_add_u64 v[212:213], s[20:21], 0, v[192:193]
	v_lshl_add_u64 v[202:203], v[220:221], 0, s[2:3]
	v_cmp_gt_u32_e32 vcc, s1, v0
	v_ashrrev_i32_e32 v209, 31, v208
	s_movk_i32 s2, 0xfe40
	global_load_dwordx4 v[38:41], v6, s[8:9]
	global_load_dwordx4 v[22:25], v7, s[8:9]
	v_add_u32_e32 v6, 0x41800, v14
	v_add_u32_e32 v7, 0x41c00, v14
	v_cndmask_b32_e32 v203, v203, v213, vcc
	v_cndmask_b32_e32 v202, v202, v212, vcc
	v_lshlrev_b64 v[230:231], 9, v[208:209]
	s_mov_b32 s3, -1
	global_load_dwordx4 v[34:37], v6, s[8:9]
	global_load_dwordx4 v[10:13], v7, s[8:9]
	v_add_u32_e32 v6, 0x42000, v14
	v_add_u32_e32 v7, 0x42400, v14
	v_add_u32_e32 v15, 0x42800, v14
	v_add_u32_e32 v18, 0x42c00, v14
	v_lshl_add_u64 v[206:207], v[202:203], 0, v[210:211]
	v_lshl_add_u64 v[224:225], v[202:203], 0, v[222:223]
	v_lshl_add_u64 v[228:229], v[202:203], 0, v[226:227]
	v_lshl_add_u64 v[202:203], v[202:203], 0, v[230:231]
	v_lshl_add_u64 v[212:213], v[212:213], 0, 64
	v_lshl_add_u64 v[220:221], v[220:221], 0, s[2:3]
	global_load_dwordx4 v[26:29], v6, s[8:9]
	s_nop 0
	global_load_dwordx4 v[6:9], v7, s[8:9]
	s_nop 0
	global_load_dwordx4 v[14:17], v15, s[8:9]
	s_nop 0
	global_load_dwordx4 v[18:21], v18, s[8:9]
	s_nop 0
	global_load_dword v208, v[206:207], off
	s_nop 0
	global_load_dword v207, v[224:225], off
	global_load_dword v204, v[228:229], off
	s_nop 0
	global_load_dword v203, v[202:203], off
	s_nop 0
	global_load_dword v206, v192, s[10:11]
	global_load_dword v202, v192, s[10:11] offset:64
	v_cndmask_b32_e32 v213, v221, v213, vcc
	v_cndmask_b32_e32 v212, v220, v212, vcc
	v_lshl_add_u64 v[210:211], v[212:213], 0, v[210:211]
	v_lshl_add_u64 v[220:221], v[212:213], 0, v[222:223]
	v_lshl_add_u64 v[222:223], v[212:213], 0, v[226:227]
	v_lshl_add_u64 v[224:225], v[212:213], 0, v[230:231]
	global_load_dword v212, v[210:211], off
	s_nop 0
	global_load_dword v211, v[220:221], off
	global_load_dword v210, v[222:223], off
	global_load_dword v209, v[224:225], off
	v_lshl_or_b32 v190, v197, 4, v1
	v_lshlrev_b32_e32 v186, 2, v190
	global_load_dword v189, v186, s[24:25]
	global_load_dword v188, v186, s[26:27]
	v_mov_b32_e32 v233, v249
	v_mov_b32_e32 v232, v248
	v_mov_b32_e32 v214, v240
	v_mov_b32_e32 v215, v241
	v_mov_b32_e32 v216, v242
	v_mov_b32_e32 v217, v243
	v_mov_b32_e32 v218, v244
	v_mov_b32_e32 v219, v245
	v_mov_b32_e32 v220, v246
	v_mov_b32_e32 v221, v247
	s_nop 1
	v_add_f32_dpp v2, v233, v233 row_ror:8 row_mask:0xf bank_mask:0xf bound_ctrl:1
	v_mov_b32_e32 v3, v2
	s_nop 1
	v_permlane16_swap_b32_e32 v2, v3
	v_add_f32_e32 v2, v2, v3
	v_mov_b32_e32 v3, v2
	s_nop 1
	v_permlane32_swap_b32_e32 v2, v3
	v_add_f32_e32 v2, v2, v3
	v_readlane_b32 s2, v232, 4
	v_readlane_b32 s4, v2, 4
	v_readlane_b32 s5, v2, 0
	v_readlane_b32 s3, v232, 0
	v_div_scale_f32 v3, s[0:1], s4, s4, 1.0
	v_rcp_f32_e32 v4, v3
	v_lshl_add_u64 v[182:183], v[182:183], 2, s[28:29]
	v_fma_f32 v2, -v3, v4, 1.0
	v_fmac_f32_e32 v4, v2, v4
	v_div_scale_f32 v2, vcc, 1.0, s4, 1.0
	v_mul_f32_e32 v5, v2, v4
	v_fma_f32 v192, -v3, v5, v2
	v_fmac_f32_e32 v5, v192, v4
	v_fma_f32 v2, -v3, v5, v2
	v_div_scale_f32 v3, s[0:1], s5, s5, 1.0
	v_rcp_f32_e32 v192, v3
	v_div_fmas_f32 v2, v2, v4, v5
	v_div_fixup_f32 v2, v2, s4, 1.0
	s_movk_i32 s0, 0xc8
	v_fma_f32 v4, -v3, v192, 1.0
	v_fmac_f32_e32 v192, v4, v192
	v_div_scale_f32 v4, vcc, 1.0, s5, 1.0
	v_mul_f32_e32 v5, v4, v192
	v_fma_f32 v213, -v3, v5, v4
	v_fmac_f32_e32 v5, v213, v192
	v_fma_f32 v3, -v3, v5, v4
	v_div_fmas_f32 v3, v3, v192, v5
	v_div_fixup_f32 v4, v3, s5, 1.0
	v_pk_mul_f32 v[216:217], v[216:217], v[4:5] op_sel_hi:[1,0]
	v_pk_mul_f32 v[214:215], v[214:215], v[4:5] op_sel_hi:[1,0]
	v_cvt_pk_f16_f32 v217, v216, v217
	v_cvt_pk_f16_f32 v216, v214, v215
	v_pk_mul_f32 v[214:215], v[220:221], v[2:3] op_sel_hi:[1,0]
	v_pk_mul_f32 v[218:219], v[218:219], v[2:3] op_sel_hi:[1,0]
	v_add_u32_e32 v3, v205, v184
	ds_read2_b32 v[220:221], v3 offset0:128 offset1:200
	v_cvt_pk_f16_f32 v215, v214, v215
	v_cvt_pk_f16_f32 v214, v218, v219
	ds_read2st64_b32 v[218:219], v3 offset1:1
	v_add_u32_e32 v192, 32, v3
	ds_write2st64_b64 v185, v[216:217], v[214:215] offset1:1
	ds_read2st64_b32 v[214:215], v192 offset0:4 offset1:5
	s_waitcnt lgkmcnt(3)
	v_subrev_f32_e32 v5, s2, v221
	v_exp_f32_e32 v5, v5
	s_waitcnt lgkmcnt(2)
	v_subrev_f32_e32 v185, s3, v218
	v_exp_f32_e32 v185, v185
	s_waitcnt lgkmcnt(0)
	v_subrev_f32_e32 v205, s2, v214
	v_mul_f32_e32 v5, v2, v5
	v_subrev_f32_e32 v192, s3, v219
	v_exp_f32_e32 v205, v205
	v_fmac_f32_e32 v5, v4, v185
	v_mov_b32_e32 v185, v193
	v_exp_f32_e32 v192, v192
	v_lshl_add_u64 v[182:183], v[182:183], 0, v[184:185]
	v_subrev_f32_e32 v185, s2, v215
	v_mul_f32_e32 v5, 0.5, v5
	v_subrev_f32_e32 v184, s3, v220
	v_exp_f32_e32 v185, v185
	global_store_dword v[182:183], v5, off
	v_mul_f32_e32 v5, v2, v205
	v_exp_f32_e32 v184, v184
	v_fmac_f32_e32 v5, v4, v192
	v_mul_f32_e32 v5, 0.5, v5
	global_store_dword v[182:183], v5, off offset:256
	v_mul_f32_e32 v5, v2, v185
	v_fmac_f32_e32 v5, v4, v184
	v_mul_f32_e32 v5, 0.5, v5
	global_store_dword v[182:183], v5, off offset:512
	v_or_b32_e32 v5, 0xc0, v196
	v_cmp_gt_u32_e32 vcc, s0, v5
	s_and_saveexec_b64 s[0:1], vcc
	s_cbranch_execz .LBB1_19
	v_add_u32_e32 v3, 0x300, v3
	ds_read2_b32 v[184:185], v3 offset1:200
	s_waitcnt lgkmcnt(0)
	v_subrev_f32_e32 v3, s3, v184
	v_subrev_f32_e32 v5, s2, v185
	v_exp_f32_e32 v184, v3
	v_exp_f32_e32 v185, v5
	v_mov_b32_e32 v5, v2
	v_pk_mul_f32 v[2:3], v[4:5], v[184:185]
	s_nop 0
	v_add_f32_e32 v2, v2, v3
	v_mul_f32_e32 v2, 0.5, v2
	global_store_dword v[182:183], v2, off offset:768
